# speedup vs baseline: 1.0088x; 1.0037x over previous
.LBB1_5:
	s_or_b64 exec, exec, s[20:21]
	v_lshrrev_b32_e32 v1, 6, v0
	v_lshl_or_b32 v2, s2, 2, v1
	s_movk_i32 s0, 0x753
	v_cmp_gt_i32_e32 vcc, s0, v2
	s_and_saveexec_b64 s[16:17], vcc
	s_cbranch_execz .LBB1_10
	v_and_b32_e32 v17, 15, v0
	v_lshlrev_b32_e32 v46, 4, v2
	v_bfe_u32 v1, v0, 4, 2
	v_or_b32_e32 v2, v46, v17
	v_lshl_or_b32 v2, v2, 3, v1
	v_ashrrev_i32_e32 v3, 31, v2
	v_lshl_add_u64 v[10:11], v[2:3], 4, s[10:11]
	global_load_dwordx4 v[2:5], v[10:11], off
	global_load_dwordx4 v[6:9], v[10:11], off offset:64
	v_lshlrev_b32_e32 v10, 3, v0
	s_movk_i32 s0, 0x78
	v_and_or_b32 v11, v10, s0, v1
	s_movk_i32 s0, 0xf0
	v_mov_b32_e32 v18, 0x80
	v_bitop3_b32 v18, v10, s0, v18 bitop3:0xc8
	s_movk_i32 s0, 0x170
	v_mov_b32_e32 v22, 0x100
	v_and_b32_e32 v16, 8, v10
	v_bitop3_b32 v22, v10, s0, v22 bitop3:0xc8
	v_lshlrev_b32_e32 v11, 4, v11
	v_or3_b32 v18, v16, v18, v1
	v_or3_b32 v22, v16, v22, v1
	global_load_dwordx4 v[12:15], v11, s[12:13]
	v_lshlrev_b32_e32 v47, 4, v18
	v_lshlrev_b32_e32 v48, 4, v22
	global_load_dwordx4 v[18:21], v47, s[12:13]
	global_load_dwordx4 v[22:25], v48, s[12:13]
	s_movk_i32 s0, 0x1f0
	v_mov_b32_e32 v26, 0x180
	v_bitop3_b32 v10, v10, s0, v26 bitop3:0xc8
	v_or3_b32 v10, v16, v10, v1
	v_lshlrev_b32_e32 v10, 4, v10
	global_load_dwordx4 v[26:29], v10, s[12:13]
	global_load_dwordx4 v[30:33], v11, s[12:13] offset:64
	global_load_dwordx4 v[34:37], v47, s[12:13] offset:64
	global_load_dwordx4 v[38:41], v48, s[12:13] offset:64
	global_load_dwordx4 v[42:45], v10, s[12:13] offset:64
	v_ashrrev_i32_e32 v47, 31, v46
	v_mov_b32_e32 v11, 0
	v_lshlrev_b32_e32 v10, 3, v1
	s_mov_b32 s3, 0xea000
	s_mov_b32 s10, 0x1d4000
	s_movk_i32 s0, 0x4e
	s_waitcnt vmcnt(7)
	v_mfma_f32_16x16x32_f16 a[0:3], v[2:5], v[12:15], 0
	v_mul_u32_u24_e32 v14, 0x7530, v17
	v_lshl_add_u64 v[12:13], v[46:47], 1, s[14:15]
	v_lshl_add_u64 v[12:13], v[12:13], 0, v[10:11]
	s_waitcnt vmcnt(6)
	v_mfma_f32_16x16x32_f16 a[4:7], v[2:5], v[18:21], 0
	v_lshlrev_b32_e32 v10, 1, v14
	v_lshl_add_u64 v[14:15], v[12:13], 0, v[10:11]
	v_add_co_u32_e32 v12, vcc, s3, v14
	s_waitcnt vmcnt(5)
	v_mfma_f32_16x16x32_f16 a[8:11], v[2:5], v[22:25], 0
	v_addc_co_u32_e32 v13, vcc, 0, v15, vcc
	v_add_co_u32_e32 v18, vcc, s10, v14
	s_waitcnt vmcnt(4)
	v_mfma_f32_16x16x32_f16 a[12:15], v[2:5], v[26:29], 0
	v_addc_co_u32_e32 v19, vcc, 0, v15, vcc
	v_add_co_u32_e32 v20, vcc, 0x2bf000, v14
	s_waitcnt vmcnt(3)
	v_mfma_f32_16x16x32_f16 a[0:3], v[6:9], v[30:33], a[0:3]
	v_or_b32_e32 v17, 64, v17
	v_addc_co_u32_e32 v21, vcc, 0, v15, vcc
	s_waitcnt vmcnt(2)
	v_mfma_f32_16x16x32_f16 a[4:7], v[6:9], v[34:37], a[4:7]
	v_cmp_gt_u32_e64 s[0:1], s0, v17
	v_mov_b32_e32 v10, v11
	s_waitcnt vmcnt(1)
	v_mfma_f32_16x16x32_f16 a[8:11], v[6:9], v[38:41], a[8:11]
	v_accvgpr_read_b32 v22, a0
	v_accvgpr_read_b32 v24, a1
	v_accvgpr_read_b32 v23, a2
	s_waitcnt vmcnt(0)
	v_mfma_f32_16x16x32_f16 a[12:15], v[6:9], v[42:45], a[12:15]
	v_accvgpr_read_b32 v25, a3
	v_accvgpr_read_b32 v26, a4
	v_accvgpr_read_b32 v27, a5
	v_accvgpr_read_b32 v28, a6
	v_accvgpr_read_b32 v29, a7
	v_accvgpr_read_b32 v30, a8
	v_accvgpr_read_b32 v31, a9
	v_accvgpr_read_b32 v32, a10
	v_accvgpr_read_b32 v33, a11
	v_accvgpr_read_b32 v34, a12
	v_accvgpr_read_b32 v35, a13
	v_accvgpr_read_b32 v36, a14
	v_accvgpr_read_b32 v37, a15
	v_cvt_pk_f16_f32 v23, v23, v25
	v_cvt_pk_f16_f32 v22, v22, v24
	v_cvt_pk_f16_f32 v25, v28, v29
	v_cvt_pk_f16_f32 v24, v26, v27
	v_cvt_pk_f16_f32 v27, v32, v33
	v_cvt_pk_f16_f32 v26, v30, v31
	v_cvt_pk_f16_f32 v29, v36, v37
	v_cvt_pk_f16_f32 v28, v34, v35
	s_mov_b64 s[26:27], exec
	s_mov_b32 s24, 0xaaaaaaaa
	s_mov_b32 s25, 0xaaaaaaaa
	s_and_b64 exec, exec, s[24:25]
	global_store_dwordx2 v[14:15], v[22:23], off
	global_store_dwordx2 v[12:13], v[24:25], off offset:1536
	global_store_dwordx2 v[18:19], v[26:27], off offset:3072
	global_store_dwordx2 v[20:21], v[28:29], off offset:512
	s_mov_b64 exec, s[26:27]
	v_mov_b32_e32 v12, v11
	v_mov_b32_e32 v13, v11
	v_mov_b32_e32 v18, v11
	v_mov_b32_e32 v19, v11
	v_mov_b32_e32 v20, v11
	v_mov_b32_e32 v21, v11
	s_and_saveexec_b64 s[10:11], s[0:1]
	s_cbranch_execz .LBB1_8
	v_lshlrev_b32_e32 v10, 3, v17
	v_and_b32_e32 v10, 0x270, v10
	v_or3_b32 v1, v16, v10, v1
	v_lshlrev_b32_e32 v1, 4, v1
	global_load_dwordx4 v[10:13], v1, s[12:13]
	global_load_dwordx4 v[18:21], v1, s[12:13] offset:64
.LBB1_8:
	s_or_b64 exec, exec, s[10:11]
	s_waitcnt vmcnt(1)
	v_mfma_f32_16x16x32_f16 a[0:3], v[2:5], v[10:13], 0
	s_waitcnt vmcnt(0)
	v_mfma_f32_16x16x32_f16 a[0:3], v[6:9], v[18:21], a[0:3]
	s_and_b64 exec, exec, s[0:1]
	s_cbranch_execz .LBB1_10
	s_mov_b64 s[0:1], 0x2bf200
	s_nop 4
	v_accvgpr_read_b32 v5, a3
	v_lshl_add_u64 v[6:7], v[14:15], 0, s[0:1]
	v_accvgpr_read_b32 v4, a2
	v_accvgpr_read_b32 v3, a1
	v_accvgpr_read_b32 v2, a0
	v_cvt_pk_f16_f32 v5, v4, v5
	v_cvt_pk_f16_f32 v4, v2, v3
	v_add_co_u32_e32 v2, vcc, 0xea000, v6
	s_nop 1
	v_addc_co_u32_e32 v3, vcc, 0, v7, vcc
	s_and_b64 exec, exec, s[24:25]
	global_store_dwordx2 v[2:3], v[4:5], off offset:1536
